# NSA phase C merge loop: 16 ushort RMW loads hoisted above the gate-load wait (vmcnt(16)), overlap with sigmoid/div math
# speedup vs baseline: 1.0008x; 1.0008x over previous
.LBB0_709:
	v_or_b32_e32 v14, s9, v190
	v_add_u32_e32 v15, s31, v14
	v_mov_b64_e32 v[10:11], s[6:7]
	v_mad_i64_i32 v[10:11], s[0:1], v15, s12, v[10:11]
	s_mov_b32 s9, s93
	v_lshl_add_u64 v[10:11], v[10:11], 0, s[8:9]
	v_add_co_u32_e32 v10, vcc, 0x2000, v10
	s_mov_b32 s9, 4
	s_nop 0
	v_addc_co_u32_e32 v11, vcc, 0, v11, vcc
	global_load_dwordx2 v[10:11], v[10:11], off offset:1936
	v_add_u32_e32 v244, s30, v15
	v_ashrrev_i32_e32 v245, 31, v244
	v_lshlrev_b64 v[244:245], 10, v[244:245]
	v_lshl_add_u64 v[244:245], v[140:141], 0, v[244:245]
	global_load_ushort v40, v[244:245], off
	global_load_ushort v41, v[244:245], off offset:128
	global_load_ushort v42, v[244:245], off offset:256
	global_load_ushort v43, v[244:245], off offset:384
	global_load_ushort v44, v[244:245], off offset:32
	global_load_ushort v45, v[244:245], off offset:160
	global_load_ushort v46, v[244:245], off offset:288
	global_load_ushort v47, v[244:245], off offset:416
	global_load_ushort v48, v[244:245], off offset:64
	global_load_ushort v49, v[244:245], off offset:192
	global_load_ushort v50, v[244:245], off offset:320
	global_load_ushort v51, v[244:245], off offset:448
	global_load_ushort v52, v[244:245], off offset:96
	global_load_ushort v53, v[244:245], off offset:224
	global_load_ushort v54, v[244:245], off offset:352
	global_load_ushort v55, v[244:245], off offset:480
	s_waitcnt vmcnt(16)
	v_lshlrev_b32_e32 v12, 16, v10
	v_and_b32_e32 v10, 0xffff0000, v10
	v_mul_f32_e32 v10, 0xbfb8aa3b, v10
	v_exp_f32_e32 v10, v10
	v_mul_f32_e32 v12, 0xbfb8aa3b, v12
	v_exp_f32_e32 v12, v12
	v_add_f32_e32 v10, 1.0, v10
	v_rcp_f32_e32 v17, v10
	v_lshlrev_b32_e32 v10, 16, v11
	v_mul_f32_e32 v10, 0xbfb8aa3b, v10
	v_exp_f32_e32 v10, v10
	v_add_f32_e32 v12, 1.0, v12
	v_rcp_f32_e32 v16, v12
	v_add_f32_e32 v10, 1.0, v10
	v_rcp_f32_e32 v18, v10
	v_and_b32_e32 v10, 0xffff0000, v11
	v_mul_f32_e32 v10, 0xbfb8aa3b, v10
	v_exp_f32_e32 v10, v10
	s_nop 0
	v_add_f32_e32 v10, 1.0, v10
	v_rcp_f32_e32 v19, v10
	v_lshl_add_u32 v10, v14, 4, 0
	v_add_u32_e32 v10, 0x10000, v10
	ds_read_b128 v[10:13], v10
	s_waitcnt lgkmcnt(0)
	v_div_scale_f32 v20, s[10:11], v10, v10, v16
	v_rcp_f32_e32 v21, v20
	v_cmp_lt_f32_e64 s[0:1], 0, v10
	v_fma_f32 v22, -v20, v21, 1.0
	v_fmac_f32_e32 v21, v22, v21
	v_div_scale_f32 v22, vcc, v16, v10, v16
	v_mul_f32_e32 v23, v22, v21
	v_fma_f32 v24, -v20, v23, v22
	v_fmac_f32_e32 v23, v24, v21
	v_fma_f32 v20, -v20, v23, v22
	v_div_fmas_f32 v20, v20, v21, v23
	v_div_fixup_f32 v10, v20, v10, v16
	v_cndmask_b32_e64 v20, 0, v10, s[0:1]
	v_div_scale_f32 v10, s[10:11], v11, v11, v17
	v_rcp_f32_e32 v16, v10
	v_cmp_lt_f32_e64 s[0:1], 0, v11
	v_lshl_add_u32 v24, v14, 10, v189
	v_fma_f32 v21, -v10, v16, 1.0
	v_fmac_f32_e32 v16, v21, v16
	v_div_scale_f32 v21, vcc, v17, v11, v17
	v_mul_f32_e32 v22, v21, v16
	v_fma_f32 v23, -v10, v22, v21
	v_fmac_f32_e32 v22, v23, v16
	v_fma_f32 v10, -v10, v22, v21
	v_div_fmas_f32 v10, v10, v16, v22
	v_div_fixup_f32 v10, v10, v11, v17
	v_cndmask_b32_e64 v21, 0, v10, s[0:1]
	v_div_scale_f32 v10, s[10:11], v12, v12, v18
	v_rcp_f32_e32 v11, v10
	v_cmp_lt_f32_e64 s[0:1], 0, v12
	v_fma_f32 v16, -v10, v11, 1.0
	v_fmac_f32_e32 v11, v16, v11
	v_div_scale_f32 v16, vcc, v18, v12, v18
	v_mul_f32_e32 v17, v16, v11
	v_fma_f32 v22, -v10, v17, v16
	v_fmac_f32_e32 v17, v22, v11
	v_fma_f32 v10, -v10, v17, v16
	v_div_fmas_f32 v10, v10, v11, v17
	v_div_fixup_f32 v10, v10, v12, v18
	v_cndmask_b32_e64 v22, 0, v10, s[0:1]
	v_div_scale_f32 v10, s[10:11], v13, v13, v19
	v_rcp_f32_e32 v11, v10
	v_cmp_lt_f32_e64 s[0:1], 0, v13
	v_fma_f32 v12, -v10, v11, 1.0
	v_fmac_f32_e32 v11, v12, v11
	v_div_scale_f32 v12, vcc, v19, v13, v19
	v_mul_f32_e32 v16, v12, v11
	v_fma_f32 v17, -v10, v16, v12
	v_fmac_f32_e32 v16, v17, v11
	v_fma_f32 v10, -v10, v16, v12
	v_div_fmas_f32 v10, v10, v11, v16
	v_div_fixup_f32 v10, v10, v13, v19
	v_cndmask_b32_e64 v23, 0, v10, s[0:1]
	v_add_u32_e32 v10, s30, v15
	v_ashrrev_i32_e32 v11, 31, v10
	v_lshlrev_b64 v[10:11], 10, v[10:11]
	v_lshl_add_u64 v[10:11], v[140:141], 0, v[10:11]
	ds_read2_b32 v[26:27], v24 offset1:16
	ds_read2_b32 v[28:29], v24 offset0:32 offset1:48
	ds_read2_b32 v[30:31], v24 offset0:64 offset1:80
	ds_read2_b32 v[32:33], v24 offset0:96 offset1:112
	ds_read2_b32 v[34:35], v24 offset0:128 offset1:144
	ds_read2_b32 v[36:37], v24 offset0:160 offset1:176
	ds_read2_b32 v[38:39], v24 offset0:192 offset1:208
	ds_read2_b32 v[56:57], v24 offset0:224 offset1:240
	s_and_b64 vcc, exec, s[4:5]
	s_mov_b64 s[4:5], 0
	s_waitcnt vmcnt(0) lgkmcnt(0)
	v_lshlrev_b32_e32 v40, 16, v40
	v_lshlrev_b32_e32 v41, 16, v41
	v_lshlrev_b32_e32 v42, 16, v42
	v_lshlrev_b32_e32 v43, 16, v43
	v_lshlrev_b32_e32 v44, 16, v44
	v_lshlrev_b32_e32 v45, 16, v45
	v_lshlrev_b32_e32 v46, 16, v46
	v_lshlrev_b32_e32 v47, 16, v47
	v_lshlrev_b32_e32 v48, 16, v48
	v_lshlrev_b32_e32 v49, 16, v49
	v_lshlrev_b32_e32 v50, 16, v50
	v_lshlrev_b32_e32 v51, 16, v51
	v_lshlrev_b32_e32 v52, 16, v52
	v_lshlrev_b32_e32 v53, 16, v53
	v_lshlrev_b32_e32 v54, 16, v54
	v_lshlrev_b32_e32 v55, 16, v55
	v_fmac_f32_e32 v40, v26, v20
	v_fmac_f32_e32 v41, v30, v21
	v_fmac_f32_e32 v42, v34, v22
	v_fmac_f32_e32 v43, v38, v23
	v_fmac_f32_e32 v44, v27, v20
	v_fmac_f32_e32 v45, v31, v21
	v_fmac_f32_e32 v46, v35, v22
	v_fmac_f32_e32 v47, v39, v23
	v_fmac_f32_e32 v48, v28, v20
	v_fmac_f32_e32 v49, v32, v21
	v_fmac_f32_e32 v50, v36, v22
	v_fmac_f32_e32 v51, v56, v23
	v_fmac_f32_e32 v52, v29, v20
	v_fmac_f32_e32 v53, v33, v21
	v_fmac_f32_e32 v54, v37, v22
	v_fmac_f32_e32 v55, v57, v23
	v_bfe_u32 v58, v40, 16, 1
	v_bfe_u32 v59, v41, 16, 1
	v_bfe_u32 v60, v42, 16, 1
	v_bfe_u32 v61, v43, 16, 1
	v_bfe_u32 v62, v44, 16, 1
	v_bfe_u32 v63, v45, 16, 1
	v_bfe_u32 v64, v46, 16, 1
	v_bfe_u32 v65, v47, 16, 1
	v_bfe_u32 v68, v48, 16, 1
	v_bfe_u32 v69, v49, 16, 1
	v_bfe_u32 v70, v50, 16, 1
	v_bfe_u32 v71, v51, 16, 1
	v_bfe_u32 v72, v52, 16, 1
	v_bfe_u32 v73, v53, 16, 1
	v_bfe_u32 v74, v54, 16, 1
	v_bfe_u32 v75, v55, 16, 1
	v_add3_u32 v40, v40, v58, s90
	v_add3_u32 v41, v41, v59, s90
	v_add3_u32 v42, v42, v60, s90
	v_add3_u32 v43, v43, v61, s90
	v_add3_u32 v44, v44, v62, s90
	v_add3_u32 v45, v45, v63, s90
	v_add3_u32 v46, v46, v64, s90
	v_add3_u32 v47, v47, v65, s90
	v_add3_u32 v48, v48, v68, s90
	v_add3_u32 v49, v49, v69, s90
	v_add3_u32 v50, v50, v70, s90
	v_add3_u32 v51, v51, v71, s90
	v_add3_u32 v52, v52, v72, s90
	v_add3_u32 v53, v53, v73, s90
	v_add3_u32 v54, v54, v74, s90
	v_add3_u32 v55, v55, v75, s90
	global_store_short_d16_hi v[10:11], v40, off
	global_store_short_d16_hi v[10:11], v41, off offset:128
	global_store_short_d16_hi v[10:11], v42, off offset:256
	global_store_short_d16_hi v[10:11], v43, off offset:384
	global_store_short_d16_hi v[10:11], v44, off offset:32
	global_store_short_d16_hi v[10:11], v45, off offset:160
	global_store_short_d16_hi v[10:11], v46, off offset:288
	global_store_short_d16_hi v[10:11], v47, off offset:416
	global_store_short_d16_hi v[10:11], v48, off offset:64
	global_store_short_d16_hi v[10:11], v49, off offset:192
	global_store_short_d16_hi v[10:11], v50, off offset:320
	global_store_short_d16_hi v[10:11], v51, off offset:448
	global_store_short_d16_hi v[10:11], v52, off offset:96
	global_store_short_d16_hi v[10:11], v53, off offset:224
	global_store_short_d16_hi v[10:11], v54, off offset:352
	global_store_short_d16_hi v[10:11], v55, off offset:480
	s_cbranch_vccnz .LBB0_709
	v_readlane_b32 s0, v254, 28
	s_add_i32 s29, s29, s0
	s_cmpk_lt_i32 s29, 0x400
	s_barrier
	s_cbranch_scc1 .LBB0_603
